# P7: activation-tile DMA groups moved from the SP2 MFMA block to the SP2 load-segment start (MFMA block pure), wait vmcnt(8+k)
# speedup vs baseline: 1.0014x; 1.0014x over previous
.Lp7vg_mmjoin_a:
	s_barrier
	s_add_u32 s2, s44, 0x1000
	s_addc_u32 s3, s45, 0
	s_mov_b32 m0, s19
	v_lshl_add_u64 v[68:69], s[44:45], 0, v[214:215]
	global_load_lds_dwordx4 v[68:69], off
	v_lshl_add_u64 v[68:69], s[44:45], 0, v[218:219]
	s_mov_b32 m0, s33
	s_nop 0
	global_load_lds_dwordx4 v[68:69], off
	v_lshl_add_u64 v[68:69], s[2:3], 0, v[214:215]
	s_mov_b32 m0, s37
	v_lshl_add_u64 v[224:225], s[4:5], 0, v[216:217]
	global_load_lds_dwordx4 v[68:69], off
	v_lshl_add_u64 v[68:69], s[2:3], 0, v[218:219]
	s_mov_b32 m0, s39
	v_cndmask_b32_e64 v66, 0, 1, s[40:41]
	global_load_lds_dwordx4 v[68:69], off
	v_lshl_add_u64 v[68:69], s[4:5], 0, v[212:213]
	s_mov_b32 m0, s15
	v_cmp_ne_u32_e64 s[2:3], 1, v66
	global_load_lds_dwordx4 v[68:69], off
	s_mov_b32 m0, s49
	s_nop 0
	global_load_lds_dwordx4 v[224:225], off
	s_andn2_b64 vcc, exec, s[40:41]
	s_cbranch_vccnz .Lhalfskip_p7a
	ds_read_b128 v[58:61], v236 offset:16384
	ds_read_b128 v[62:65], v236 offset:17408
	ds_read_b128 v[50:53], v236 offset:18432
	ds_read_b128 v[54:57], v236 offset:19456
	ds_read_b128 v[42:45], v236 offset:20480
	ds_read_b128 v[46:49], v236 offset:21504
	ds_read_b128 v[34:37], v236 offset:22528
	ds_read_b128 v[38:41], v236 offset:23552
.Lhalfskip_p7a:
	s_cmp_eq_u32 s100, 3
	s_cbranch_scc1 .Lp7dma_w5_a
	s_cmp_eq_u32 s100, 2
	s_cbranch_scc1 .Lp7dma_wk2_a
	s_waitcnt vmcnt(8)
	s_branch .Lp7dma_wd_a

.Lp7vg_mmjoin_b:
	s_barrier
	v_lshl_add_u64 v[240:241], s[46:47], 0, v[214:215]
	s_add_i32 m0, s15, 0x18000
	s_nop 0
	global_load_lds_dwordx4 v[240:241], off
	s_add_i32 m0, s15, 0x1a000
	v_lshl_add_u64 v[240:241], s[46:47], 0, v[218:219]
	global_load_lds_dwordx4 v[240:241], off
	s_add_u32 s44, s44, 0x85000
	s_addc_u32 s45, s45, 0
	v_lshl_add_u64 v[240:241], s[44:45], 0, v[214:215]
	s_add_i32 m0, s15, 0x1c000
	v_lshl_add_u64 v[68:69], v[68:69], 0, s[10:11]
	global_load_lds_dwordx4 v[240:241], off
	v_lshl_add_u64 v[240:241], s[44:45], 0, v[218:219]
	s_add_i32 m0, s15, 0x1e000
	s_nop 0
	global_load_lds_dwordx4 v[240:241], off
	s_mov_b32 m0, s54
	s_nop 0
	global_load_lds_dwordx4 v[68:69], off
	v_lshl_add_u64 v[68:69], v[224:225], 0, s[10:11]
	s_mov_b32 m0, s55
	s_nop 0
	global_load_lds_dwordx4 v[68:69], off
	s_and_b64 vcc, exec, s[2:3]
	s_cbranch_vccnz .Lhalfskip_p7b
	ds_read_b128 v[58:61], v236 offset:49152
	ds_read_b128 v[62:65], v236 offset:50176
	ds_read_b128 v[50:53], v236 offset:51200
	ds_read_b128 v[54:57], v236 offset:52224
	ds_read_b128 v[42:45], v236 offset:53248
	ds_read_b128 v[46:49], v236 offset:54272
	ds_read_b128 v[34:37], v236 offset:55296
	ds_read_b128 v[38:41], v236 offset:56320

.Lp7dma_skip_d:
	s_branch .LBB0_781
.LBB0_798:
	s_and_b64 vcc, exec, s[12:13]
	s_cbranch_vccz .LBB0_800
	s_barrier
